# baseline (speedup 1.0000x reference)
.LBB3_1:
	s_lshl_b32 s12, s3, 15
	v_or_b32_e32 v67, s12, v65
	s_waitcnt lgkmcnt(0)
	v_mfma_f32_16x16x32_f16 v[54:57], v[22:25], v[10:13], v[54:57]
	ds_read_b128 v[68:71], v67 offset:1024
	ds_read_b128 v[72:75], v67 offset:3072
	v_or_b32_e32 v67, s12, v64
	v_mfma_f32_16x16x32_f16 v[50:53], v[18:21], v[10:13], v[50:53]
	ds_read_b128 v[76:79], v67 offset:17408
	ds_read_b128 v[80:83], v67 offset:19456
	s_add_i32 s3, s3, 1
	v_mfma_f32_16x16x32_f16 v[46:49], v[26:29], v[10:13], v[46:49]
	ds_read_b128 v[84:87], v67 offset:21504
	ds_read_b128 v[88:91], v67 offset:23552
	v_mfma_f32_16x16x32_f16 v[42:45], v[14:17], v[10:13], v[42:45]
	v_mfma_f32_16x16x32_f16 v[38:41], v[22:25], v[6:9], v[38:41]
	v_mfma_f32_16x16x32_f16 v[34:37], v[18:21], v[6:9], v[34:37]
	v_mfma_f32_16x16x32_f16 v[30:33], v[26:29], v[6:9], v[30:33]
	v_mfma_f32_16x16x32_f16 v[2:5], v[14:17], v[6:9], v[2:5]
	v_or_b32_e32 v10, s12, v66
	v_lshl_add_u64 v[6:7], v[60:61], 0, s[4:5]
	v_readfirstlane_b32 s12, v10
	v_lshl_add_u64 v[8:9], v[6:7], 0, s[6:7]
	s_mov_b32 m0, s12
	s_waitcnt vmcnt(4) lgkmcnt(0)
	s_barrier
	global_load_lds_dwordx4 v[8:9], off
	v_or_b32_e32 v8, 0x2000, v10
	v_lshl_add_u64 v[6:7], v[6:7], 0, s[10:11]
	v_readfirstlane_b32 s12, v8
	s_mov_b32 m0, s12
	v_or_b32_e32 v11, 0x4000, v10
	global_load_lds_dwordx4 v[6:7], off
	v_lshl_add_u64 v[6:7], v[58:59], 0, s[4:5]
	v_readfirstlane_b32 s12, v11
	v_lshl_add_u64 v[8:9], v[6:7], 0, s[6:7]
	s_mov_b32 m0, s12
	v_lshl_add_u64 v[6:7], v[6:7], 0, s[10:11]
	global_load_lds_dwordx4 v[8:9], off
	v_or_b32_e32 v8, 0x6000, v10
	s_cmp_lg_u32 s3, 3
	v_readfirstlane_b32 s12, v8
	s_mov_b32 m0, s12
	s_cselect_b32 s3, s3, 0
	global_load_lds_dwordx4 v[6:7], off
	s_lshl_b32 s12, s3, 15
	v_or_b32_e32 v6, s12, v65
	v_or_b32_e32 v14, s12, v64
	s_waitcnt lgkmcnt(0)
	v_mfma_f32_16x16x32_f16 v[54:57], v[76:79], v[68:71], v[54:57]
	ds_read_b128 v[10:13], v6
	ds_read_b128 v[6:9], v6 offset:2048
	v_mfma_f32_16x16x32_f16 v[50:53], v[80:83], v[68:71], v[50:53]
	ds_read_b128 v[22:25], v14 offset:16384
	ds_read_b128 v[18:21], v14 offset:18432
	v_mfma_f32_16x16x32_f16 v[46:49], v[84:87], v[68:71], v[46:49]
	ds_read_b128 v[26:29], v14 offset:20480
	ds_read_b128 v[14:17], v14 offset:22528
	v_mfma_f32_16x16x32_f16 v[42:45], v[88:91], v[68:71], v[42:45]
	v_mfma_f32_16x16x32_f16 v[38:41], v[76:79], v[72:75], v[38:41]
	v_mfma_f32_16x16x32_f16 v[34:37], v[80:83], v[72:75], v[34:37]
	v_mfma_f32_16x16x32_f16 v[30:33], v[84:87], v[72:75], v[30:33]
	v_mfma_f32_16x16x32_f16 v[2:5], v[88:91], v[72:75], v[2:5]
	s_add_u32 s4, s4, 0x80
	s_addc_u32 s5, s5, 0
	s_cmpk_eq_i32 s4, 0x680
	s_cbranch_scc0 .LBB3_1
	s_waitcnt lgkmcnt(0)
	v_mfma_f32_16x16x32_f16 v[54:57], v[22:25], v[10:13], v[54:57]
	ds_read_b128 v[58:61], v65 offset:33792
	ds_read_b128 v[66:69], v65 offset:35840
	v_mfma_f32_16x16x32_f16 v[50:53], v[18:21], v[10:13], v[50:53]
	ds_read_b128 v[70:73], v64 offset:50176
	ds_read_b128 v[74:77], v64 offset:52224
	v_mfma_f32_16x16x32_f16 v[46:49], v[26:29], v[10:13], v[46:49]
	ds_read_b128 v[78:81], v64 offset:54272
	ds_read_b128 v[82:85], v64 offset:56320
	v_mfma_f32_16x16x32_f16 v[10:13], v[14:17], v[10:13], v[42:45]
	v_mfma_f32_16x16x32_f16 v[22:25], v[22:25], v[6:9], v[38:41]
	v_mfma_f32_16x16x32_f16 v[18:21], v[18:21], v[6:9], v[34:37]
	v_mfma_f32_16x16x32_f16 v[26:29], v[26:29], v[6:9], v[30:33]
	v_mfma_f32_16x16x32_f16 v[2:5], v[14:17], v[6:9], v[2:5]
	v_or_b32_e32 v14, 0x10000, v65
	s_nop 0
	v_add_u32_e32 v30, 0x10800, v65
	s_waitcnt vmcnt(4) lgkmcnt(0)
	s_barrier
	s_waitcnt lgkmcnt(0)
	v_mfma_f32_16x16x32_f16 v[6:9], v[70:73], v[58:61], v[54:57]
	ds_read_b128 v[14:17], v14
	ds_read_b128 v[30:33], v30
	v_or_b32_e32 v38, 0x14000, v64
	v_mfma_f32_16x16x32_f16 v[34:37], v[74:77], v[58:61], v[50:53]
	v_add_u32_e32 v42, 0x14800, v64
	v_add_u32_e32 v54, 0x15800, v64
	ds_read_b128 v[38:41], v38
	v_add_u32_e32 v50, 0x15000, v64
	ds_read_b128 v[42:45], v42
	v_mfma_f32_16x16x32_f16 v[46:49], v[78:81], v[58:61], v[46:49]
	ds_read_b128 v[50:53], v50
	ds_read_b128 v[54:57], v54
	v_mfma_f32_16x16x32_f16 v[10:13], v[82:85], v[58:61], v[10:13]
	v_mfma_f32_16x16x32_f16 v[22:25], v[70:73], v[66:69], v[22:25]
	v_mfma_f32_16x16x32_f16 v[18:21], v[74:77], v[66:69], v[18:21]
	v_mfma_f32_16x16x32_f16 v[26:29], v[78:81], v[66:69], v[26:29]
	v_mfma_f32_16x16x32_f16 v[2:5], v[82:85], v[66:69], v[2:5]
	v_add_u32_e32 v58, 0x10400, v65
	v_add_u32_e32 v66, 0x10c00, v65
	v_add_u32_e32 v70, 0x14400, v64
	v_add_u32_e32 v74, 0x14c00, v64
	v_add_u32_e32 v78, 0x15400, v64
	v_add_u32_e32 v82, 0x15c00, v64
	s_waitcnt lgkmcnt(0)
	v_mfma_f32_16x16x32_f16 v[6:9], v[38:41], v[14:17], v[6:9]
	ds_read_b128 v[58:61], v58
	ds_read_b128 v[66:69], v66
	v_mfma_f32_16x16x32_f16 v[34:37], v[42:45], v[14:17], v[34:37]
	ds_read_b128 v[70:73], v70
	ds_read_b128 v[74:77], v74
	v_mfma_f32_16x16x32_f16 v[46:49], v[50:53], v[14:17], v[46:49]
	ds_read_b128 v[78:81], v78
	ds_read_b128 v[82:85], v82
	v_mfma_f32_16x16x32_f16 v[10:13], v[54:57], v[14:17], v[10:13]
	v_mfma_f32_16x16x32_f16 v[14:17], v[38:41], v[30:33], v[22:25]
	v_mfma_f32_16x16x32_f16 v[18:21], v[42:45], v[30:33], v[18:21]
	v_mfma_f32_16x16x32_f16 v[22:25], v[50:53], v[30:33], v[26:29]
	v_mfma_f32_16x16x32_f16 v[2:5], v[54:57], v[30:33], v[2:5]
	s_waitcnt vmcnt(0) lgkmcnt(0)
	s_waitcnt lgkmcnt(0)
	v_mfma_f32_16x16x32_f16 v[6:9], v[70:73], v[58:61], v[6:9]
	s_barrier
	ds_read_b128 v[26:29], v65
	ds_read_b128 v[30:33], v65 offset:2048
	v_mfma_f32_16x16x32_f16 v[34:37], v[74:77], v[58:61], v[34:37]
	ds_read_b128 v[38:41], v64 offset:16384
	ds_read_b128 v[42:45], v64 offset:18432
	v_mfma_f32_16x16x32_f16 v[46:49], v[78:81], v[58:61], v[46:49]
	ds_read_b128 v[50:53], v64 offset:20480
	ds_read_b128 v[54:57], v64 offset:22528
	v_mfma_f32_16x16x32_f16 v[10:13], v[82:85], v[58:61], v[10:13]
	v_mfma_f32_16x16x32_f16 v[14:17], v[70:73], v[66:69], v[14:17]
	v_mfma_f32_16x16x32_f16 v[18:21], v[74:77], v[66:69], v[18:21]
	v_mfma_f32_16x16x32_f16 v[22:25], v[78:81], v[66:69], v[22:25]
	v_mfma_f32_16x16x32_f16 v[2:5], v[82:85], v[66:69], v[2:5]
	s_waitcnt lgkmcnt(0)
	v_mfma_f32_16x16x32_f16 v[6:9], v[38:41], v[26:29], v[6:9]
	ds_read_b128 v[58:61], v64 offset:19456
	s_lshl_b64 s[0:1], s[0:1], 2
	v_lshl_add_u32 v63, v63, 5, s2
	v_mfma_f32_16x16x32_f16 v[34:37], v[42:45], v[26:29], v[34:37]
	s_add_u32 s0, s8, s0
	v_and_or_b32 v0, v0, 15, v63
	s_addc_u32 s1, s9, s1
	v_mfma_f32_16x16x32_f16 v[46:49], v[50:53], v[26:29], v[46:49]
	v_and_b32_e32 v1, 12, v1
	v_mfma_f32_16x16x32_f16 v[10:13], v[54:57], v[26:29], v[10:13]
	ds_read_b128 v[26:29], v65 offset:1024
	v_mfma_f32_16x16x32_f16 v[14:17], v[38:41], v[30:33], v[14:17]
	ds_read_b128 v[38:41], v65 offset:3072
	v_mfma_f32_16x16x32_f16 v[18:21], v[42:45], v[30:33], v[18:21]
	ds_read_b128 v[42:45], v64 offset:17408
	v_mfma_f32_16x16x32_f16 v[22:25], v[50:53], v[30:33], v[22:25]
	ds_read_b128 v[50:53], v64 offset:21504
	ds_read_b128 v[64:67], v64 offset:23552
	v_mfma_f32_16x16x32_f16 v[2:5], v[54:57], v[30:33], v[2:5]
	s_waitcnt lgkmcnt(0)
	v_mfma_f32_16x16x32_f16 v[6:9], v[42:45], v[26:29], v[6:9]
	v_mfma_f32_16x16x32_f16 v[34:37], v[58:61], v[26:29], v[34:37]
	v_mfma_f32_16x16x32_f16 v[46:49], v[50:53], v[26:29], v[46:49]
	v_mfma_f32_16x16x32_f16 v[10:13], v[64:67], v[26:29], v[10:13]
	v_mfma_f32_16x16x32_f16 v[14:17], v[42:45], v[38:41], v[14:17]
	v_mfma_f32_16x16x32_f16 v[18:21], v[58:61], v[38:41], v[18:21]
	v_mfma_f32_16x16x32_f16 v[22:25], v[50:53], v[38:41], v[22:25]
	v_mfma_f32_16x16x32_f16 v[2:5], v[64:67], v[38:41], v[2:5]
	v_and_b32_e32 v68, 8, v0
	v_cmp_eq_u32_e32 vcc, 0, v68
	v_lshlrev_b32_e32 v72, 3, v68
	v_lshl_add_u32 v72, v1, 2, v72
	v_lshl_add_u32 v72, v62, 8, v72
	v_mov_b32_e32 v73, 0
	v_lshl_add_u64 v[30:31], s[0:1], 0, v[72:73]
	v_and_b32_e32 v70, 0xfffffff7, v0
	v_mov_b32_e32 v71, 0
	v_lshlrev_b64 v[70:71], 12, v[70:71]
	v_lshl_add_u64 v[30:31], v[30:31], 0, v[70:71]
	s_mov_b64 s[4:5], 0x8000
	v_lshl_add_u64 v[32:33], v[30:31], 0, s[4:5]
	s_mov_b64 s[4:5], 0x10000
	v_lshl_add_u64 v[54:55], v[30:31], 0, s[4:5]
	s_mov_b64 s[4:5], 0x18000
	v_lshl_add_u64 v[56:57], v[30:31], 0, s[4:5]
	v_cndmask_b32_dpp v74, v34, v6, vcc row_ror:8 row_mask:0xf bank_mask:0xf
	v_cndmask_b32_dpp v75, v35, v7, vcc row_ror:8 row_mask:0xf bank_mask:0xf
	v_cndmask_b32_dpp v76, v36, v8, vcc row_ror:8 row_mask:0xf bank_mask:0xf
	v_cndmask_b32_dpp v77, v37, v9, vcc row_ror:8 row_mask:0xf bank_mask:0xf
	v_cndmask_b32_dpp v78, v10, v46, vcc row_ror:8 row_mask:0xf bank_mask:0xf
	v_cndmask_b32_dpp v79, v11, v47, vcc row_ror:8 row_mask:0xf bank_mask:0xf
	v_cndmask_b32_dpp v80, v12, v48, vcc row_ror:8 row_mask:0xf bank_mask:0xf
	v_cndmask_b32_dpp v81, v13, v49, vcc row_ror:8 row_mask:0xf bank_mask:0xf
	v_cndmask_b32_dpp v82, v18, v14, vcc row_ror:8 row_mask:0xf bank_mask:0xf
	v_cndmask_b32_dpp v83, v19, v15, vcc row_ror:8 row_mask:0xf bank_mask:0xf
	v_cndmask_b32_dpp v84, v20, v16, vcc row_ror:8 row_mask:0xf bank_mask:0xf
	v_cndmask_b32_dpp v85, v21, v17, vcc row_ror:8 row_mask:0xf bank_mask:0xf
	v_cndmask_b32_dpp v86, v2, v22, vcc row_ror:8 row_mask:0xf bank_mask:0xf
	v_cndmask_b32_dpp v87, v3, v23, vcc row_ror:8 row_mask:0xf bank_mask:0xf
	v_cndmask_b32_dpp v88, v4, v24, vcc row_ror:8 row_mask:0xf bank_mask:0xf
	v_cndmask_b32_dpp v89, v5, v25, vcc row_ror:8 row_mask:0xf bank_mask:0xf
	s_not_b64 vcc, vcc
	global_store_dwordx4 v[30:31], v[74:77], off sc1
	global_store_dwordx4 v[30:31], v[78:81], off offset:128 sc1
	global_store_dwordx4 v[54:55], v[82:85], off sc1
	global_store_dwordx4 v[54:55], v[86:89], off offset:128 sc1
	v_cndmask_b32_dpp v34, v6, v34, vcc row_ror:8 row_mask:0xf bank_mask:0xf
	v_cndmask_b32_dpp v35, v7, v35, vcc row_ror:8 row_mask:0xf bank_mask:0xf
	v_cndmask_b32_dpp v36, v8, v36, vcc row_ror:8 row_mask:0xf bank_mask:0xf
	v_cndmask_b32_dpp v37, v9, v37, vcc row_ror:8 row_mask:0xf bank_mask:0xf
	v_cndmask_b32_dpp v10, v46, v10, vcc row_ror:8 row_mask:0xf bank_mask:0xf
	v_cndmask_b32_dpp v11, v47, v11, vcc row_ror:8 row_mask:0xf bank_mask:0xf
	v_cndmask_b32_dpp v12, v48, v12, vcc row_ror:8 row_mask:0xf bank_mask:0xf
	v_cndmask_b32_dpp v13, v49, v13, vcc row_ror:8 row_mask:0xf bank_mask:0xf
	v_cndmask_b32_dpp v18, v14, v18, vcc row_ror:8 row_mask:0xf bank_mask:0xf
	v_cndmask_b32_dpp v19, v15, v19, vcc row_ror:8 row_mask:0xf bank_mask:0xf
	v_cndmask_b32_dpp v20, v16, v20, vcc row_ror:8 row_mask:0xf bank_mask:0xf
	v_cndmask_b32_dpp v21, v17, v21, vcc row_ror:8 row_mask:0xf bank_mask:0xf
	v_cndmask_b32_dpp v2, v22, v2, vcc row_ror:8 row_mask:0xf bank_mask:0xf
	v_cndmask_b32_dpp v3, v23, v3, vcc row_ror:8 row_mask:0xf bank_mask:0xf
	v_cndmask_b32_dpp v4, v24, v4, vcc row_ror:8 row_mask:0xf bank_mask:0xf
	v_cndmask_b32_dpp v5, v25, v5, vcc row_ror:8 row_mask:0xf bank_mask:0xf
	global_store_dwordx4 v[32:33], v[34:37], off sc1
	global_store_dwordx4 v[32:33], v[10:13], off offset:128 sc1
	global_store_dwordx4 v[56:57], v[18:21], off sc1
	global_store_dwordx4 v[56:57], v[2:5], off offset:128 sc1
	s_endpgm

	.amdhsa_kernel _Z9gemm_gldsILi128ELi128ELi4ELi2ELi3ELi8ELi4ELi1ELi4096ELi1024ELi1024EEvPKDF16_S1_PfPKfS4_PKiPDF16_S7_S7_
		.amdhsa_group_segment_fixed_size 98304
		.amdhsa_private_segment_fixed_size 0
		.amdhsa_kernarg_size 72
		.amdhsa_user_sgpr_count 2
		.amdhsa_user_sgpr_dispatch_ptr 0
		.amdhsa_user_sgpr_queue_ptr 0
		.amdhsa_user_sgpr_kernarg_segment_ptr 1
		.amdhsa_user_sgpr_dispatch_id 0
		.amdhsa_user_sgpr_kernarg_preload_length 0
		.amdhsa_user_sgpr_kernarg_preload_offset 0
		.amdhsa_user_sgpr_private_segment_size 0
		.amdhsa_uses_dynamic_stack 0
		.amdhsa_enable_private_segment 0
		.amdhsa_system_sgpr_workgroup_id_x 1
		.amdhsa_system_sgpr_workgroup_id_y 0
		.amdhsa_system_sgpr_workgroup_id_z 0
		.amdhsa_system_sgpr_workgroup_info 0
		.amdhsa_system_vgpr_workitem_id 0
		.amdhsa_next_free_vgpr 169
		.amdhsa_next_free_sgpr 96
		.amdhsa_accum_offset 92
		.amdhsa_reserve_vcc 1
		.amdhsa_float_round_mode_32 0
		.amdhsa_float_round_mode_16_64 0
		.amdhsa_float_denorm_mode_32 3
		.amdhsa_float_denorm_mode_16_64 3
		.amdhsa_dx10_clamp 1
		.amdhsa_ieee_mode 1
		.amdhsa_fp16_overflow 0
		.amdhsa_tg_split 0
		.amdhsa_exception_fp_ieee_invalid_op 0
		.amdhsa_exception_fp_denorm_src 0
		.amdhsa_exception_fp_ieee_div_zero 0
		.amdhsa_exception_fp_ieee_overflow 0
		.amdhsa_exception_fp_ieee_underflow 0
		.amdhsa_exception_fp_ieee_inexact 0
		.amdhsa_exception_int_div_zero 0
	.end_amdhsa_kernel
